# K5 final output store made write-through (sc1)
# baseline (speedup 1.0000x reference)
.LBB3_4:
	s_or_b64 exec, exec, s[2:3]
	v_lshlrev_b32_e32 v38, 2, v38
	s_waitcnt lgkmcnt(0)
	s_barrier
	s_waitcnt vmcnt(12)
	ds_read_b128 v[40:43], v38 offset:4096
	ds_read_b128 v[44:47], v38 offset:4112
	v_cmp_eq_u32_e32 vcc, 0, v59
	v_lshlrev_b32_e32 v1, 10, v1
	s_ashr_i32 s4, s14, 5
	s_waitcnt vmcnt(6) lgkmcnt(1)
	v_mul_f32_e32 v40, v22, v40
	s_and_b32 s2, s14, 0x1f0
	s_mov_b32 s3, 0
	s_waitcnt vmcnt(2)
	v_mfma_f32_16x16x4_f32 a[0:3], v40, v34, 0
	v_mul_f32_e32 v34, v23, v41
	s_waitcnt vmcnt(0)
	v_cndmask_b32_e32 v40, 0, v62, vcc
	s_lshl_b32 s2, s2, 2
	v_mfma_f32_16x16x4_f32 a[4:7], v34, v35, 0
	v_mul_f32_e32 v34, v24, v42
	s_nop 1
	v_mfma_f32_16x16x4_f32 a[0:3], v34, v36, a[0:3]
	v_mul_f32_e32 v34, v25, v43
	s_nop 1
	v_mfma_f32_16x16x4_f32 a[4:7], v34, v37, a[4:7]
	s_waitcnt lgkmcnt(0)
	v_mul_f32_e32 v34, v18, v44
	s_nop 1
	v_mfma_f32_16x16x4_f32 a[0:3], v34, v30, a[0:3]
	v_mul_f32_e32 v30, v19, v45
	s_nop 1
	v_mfma_f32_16x16x4_f32 a[4:7], v30, v31, a[4:7]
	v_mul_f32_e32 v30, v20, v46
	s_nop 1
	v_mfma_f32_16x16x4_f32 a[0:3], v30, v32, a[0:3]
	v_mul_f32_e32 v30, v21, v47
	s_nop 1
	v_mfma_f32_16x16x4_f32 a[4:7], v30, v33, a[4:7]
	ds_read_b128 v[30:33], v38 offset:4128
	ds_read_b128 v[34:37], v38 offset:4144
	s_waitcnt lgkmcnt(1)
	v_mul_f32_e32 v30, v10, v30
	s_waitcnt lgkmcnt(0)
	v_mul_f32_e32 v34, v6, v34
	v_mfma_f32_16x16x4_f32 a[0:3], v30, v26, a[0:3]
	v_mul_f32_e32 v26, v11, v31
	s_nop 1
	v_mfma_f32_16x16x4_f32 a[4:7], v26, v27, a[4:7]
	v_mul_f32_e32 v26, v12, v32
	s_nop 1
	v_mfma_f32_16x16x4_f32 a[0:3], v26, v28, a[0:3]
	v_mul_f32_e32 v26, v13, v33
	ds_read_b128 v[30:33], v38 offset:4368
	s_waitcnt lgkmcnt(0)
	v_mul_f32_e32 v19, v19, v31
	v_mfma_f32_16x16x4_f32 a[4:7], v26, v29, a[4:7]
	ds_read_b128 v[26:29], v38 offset:4352
	v_fmac_f32_e32 v19, v18, v30
	v_fmac_f32_e32 v19, v20, v32
	v_fmac_f32_e32 v19, v21, v33
	s_waitcnt lgkmcnt(0)
	v_mul_f32_e32 v23, v23, v27
	v_fmac_f32_e32 v23, v22, v26
	v_mfma_f32_16x16x4_f32 a[0:3], v34, v14, a[0:3]
	v_mul_f32_e32 v14, v7, v35
	v_fmac_f32_e32 v23, v24, v28
	v_fmac_f32_e32 v23, v25, v29
	v_add_f32_e32 v26, v40, v23
	ds_read_b128 v[22:25], v38 offset:4384
	v_mfma_f32_16x16x4_f32 a[4:7], v14, v15, a[4:7]
	v_add_f32_e32 v15, v26, v19
	ds_read_b128 v[18:21], v38 offset:4400
	v_mul_f32_e32 v14, v8, v36
	s_waitcnt lgkmcnt(1)
	v_mul_f32_e32 v11, v11, v23
	v_fmac_f32_e32 v11, v10, v22
	v_fmac_f32_e32 v11, v12, v24
	s_waitcnt lgkmcnt(0)
	v_mul_f32_e32 v7, v7, v19
	v_mfma_f32_16x16x4_f32 a[0:3], v14, v16, a[0:3]
	v_fmac_f32_e32 v7, v6, v18
	v_fmac_f32_e32 v11, v13, v25
	v_fmac_f32_e32 v7, v8, v20
	v_add_f32_e32 v11, v15, v11
	v_fmac_f32_e32 v7, v9, v21
	v_mul_f32_e32 v10, v9, v37
	v_add_f32_e32 v6, v11, v7
	v_mov_b32_e32 v7, 1.0
	v_mfma_f32_16x16x4_f32 a[4:7], v10, v17, a[4:7]
	v_lshlrev_b32_e32 v38, 2, v56
	v_mfma_f32_16x16x4_f32 a[0:3], v6, v7, a[0:3]
	s_nop 7
	v_accvgpr_read_b32 v9, a5
	v_accvgpr_read_b32 v8, a4
	v_accvgpr_read_b32 v7, a1
	v_accvgpr_read_b32 v6, a0
	v_pk_add_f32 v[6:7], v[8:9], v[6:7]
	s_nop 0
	v_max_f32_e32 v6, 0, v6
	s_nop 1
	v_mfma_f32_16x16x4_f32 a[8:11], v2, v6, 0
	v_max_f32_e32 v2, 0, v7
	v_accvgpr_read_b32 v7, a3
	v_accvgpr_read_b32 v6, a2
	v_mfma_f32_16x16x4_f32 a[8:11], v3, v2, a[8:11]
	v_accvgpr_read_b32 v3, a7
	v_accvgpr_read_b32 v2, a6
	v_add_f32_e64 v2, v2, v6
	v_add_f32_e64 v3, v3, v7
	v_max_f32_e32 v2, 0, v2
	s_nop 1
	v_mfma_f32_16x16x4_f32 a[0:3], v4, v2, a[8:11]
	v_max_f32_e32 v2, 0, v3
	v_lshlrev_b32_e32 v3, 6, v57
	v_or3_b32 v1, v1, v3, v38
	v_mfma_f32_16x16x4_f32 a[0:3], v5, v2, a[0:3]
	s_nop 9
	ds_write_b32 v1, a0
	ds_write_b32 v1, a1 offset:64
	ds_write_b32 v1, a2 offset:128
	ds_write_b32 v1, a3 offset:192
	v_lshlrev_b32_e32 v1, 2, v0
	s_waitcnt lgkmcnt(0)
	s_barrier
	v_lshl_or_b32 v2, v0, 6, v38
	ds_read2st64_b32 v[8:9], v2 offset1:4
	ds_read2st64_b32 v[2:3], v2 offset0:8 offset1:12
	v_and_or_b32 v0, s4, -16, v0
	v_ashrrev_i32_e32 v1, 31, v0
	v_lshlrev_b64 v[0:1], 11, v[0:1]
	s_waitcnt lgkmcnt(1)
	v_mov_b32_e32 v4, v8
	s_waitcnt lgkmcnt(0)
	v_mov_b32_e32 v5, v2
	v_mov_b32_e32 v2, v9
	v_lshl_add_u64 v[0:1], s[0:1], 0, v[0:1]
	v_pk_add_f32 v[2:3], v[4:5], v[2:3]
	v_lshl_add_u64 v[0:1], v[0:1], 0, s[2:3]
	v_add_f32_e32 v2, v2, v3
	v_lshl_add_u64 v[0:1], v[0:1], 0, v[38:39]
	s_waitcnt vmcnt(0)
	v_add_f32_e32 v2, v63, v2
	global_store_dword v[0:1], v2, off sc1
	s_endpgm
